# P8 K-loop: the two A half-tile pairs leave the MFMA intervals (all four LDS-DMA pieces per load interval, as in the other GEMM phases)
# speedup vs baseline: 1.0072x; 1.0072x over previous
; #define PG8_STAGE(bufoff, gbase, voff) do { PG8_GLDS((const char*)(gbase), (voff)[0], ldsb + (bufoff)); PG8_GLDS((const char*)(gbase), (voff)[1], ldsb + (bufoff) + 8192u); } while (0)
; #define PG8_STAGEA(bufoff, gbase, o0, o1) do { PG8_GLDS((const char*)(gbase), (o0), ldsb + (bufoff)); PG8_GLDS((const char*)(gbase), (o1), ldsb + (bufoff) + 8192u); } while (0)
; #define PG8_STAGEA1(bufoff, gbase) do { if constexpr (Sched::GATHER) { PG8_STAGEA(bufoff, gbase, vA2, vA3); } else { PG8_STAGEA(bufoff, (gbase) + hstep, vA0, vA1); } } while (0)
; #define PG8_LDA(dst, b, h) do { if constexpr (F8) { _Pragma("unroll") for (int m = 0; m < 4; ++m) dst##8[m] = PG8_LD32(lds + PG8_SA(b, h) + aoff + m * 2048); } else { \
;         _Pragma("unroll") for (int m = 0; m < 4; ++m) _Pragma("unroll") for (int k = 0; k < 2; ++k) dst[m][k] = *(const LAS bf16x8*)(lds + PG8_SA(b, h) + aoff + m * 2048 + k * 1024); } } while (0)
; #define PG8_WAIT_VR() PG8_WAIT_V(8)
; #define PG8_WAIT_VX() do { if (relax) asm volatile("s_waitcnt vmcnt(%0)" :: "n"(8 + Epi::RELAX) : "memory"); else PG8_WAIT_V(8); } while (0)
; #define PG8_WAIT_L(n) asm volatile("s_waitcnt lgkmcnt(" #n ")" ::: "memory")
; template <class Epi, class Sched, bool F8 = false, bool PF = false, bool I8 = false, int PID = -1>
; __device__ __forceinline__ void gemm_phase(LAS unsigned char* lds, LAS unsigned char* xlds, const int RP, const int RPB, const int nt, const Sched& S, const Epi& E, const int stagger_ticks) {
;     ...
;             PG8_WAIT_VX(); PG8_WAIT_L(0); PG8_BAR; PG8_MMA(0, 0, At, B0); PG8_MMA(0, 1, At, B1); PG8_BAR; PG8_SCHED;
;             if constexpr (Epi::BIAS_DMA) { if (t == 0 && has_next) E.bias_dma(nxt, xlds + 8192 + ((ui + 1) & 1) * Epi::BIAS_STRIDE, wid, lane); }
;             PG8_LDA(At, 0, 1); PG8_STAGE(PG8_SB(0, 0), b2, voffB); PG8_STAGE(PG8_SB(0, 1), b2 + hstepB, voffB); PG8_STAGEA(PG8_SA(0, 0), a2, vA0, vA1);
;             PG8_WAIT_VX(); PG8_WAIT_L(0); PG8_BAR; PG8_MMA(1, 0, At, B0); PG8_MMA(1, 1, At, B1); PG8_BAR; PG8_SCHED;
;             PG8_LDB(B0, 1, 0); PG8_LDB(B1, 1, 1); PG8_SCHED; PG8_LDA(At, 1, 0); PG8_STAGEA1(PG8_SA(0, 1), a2);
;             PG8_WAIT_VR(); PG8_WAIT_L(0); PG8_BAR; PG8_MMA(0, 0, At, B0); PG8_MMA(0, 1, At, B1); PG8_BAR; PG8_SCHED;
;             PG8_LDA(At, 1, 1); PG8_STAGE(PG8_SB(1, 0), b3, voffB); PG8_STAGE(PG8_SB(1, 1), b3 + hstepB, voffB); PG8_STAGEA(PG8_SA(1, 0), a3, vA0, vA1);
.LBB0_958:
	s_add_u32 s28, s2, 0x80
	s_addc_u32 s29, s3, 0
	s_and_b64 s[24:25], s[26:27], exec
	s_cselect_b32 s28, s20, s28
	s_cselect_b32 s29, s21, s29
	s_add_u32 s24, s28, 0x80
	s_addc_u32 s25, s29, 0
	s_waitcnt vmcnt(8)
	s_and_b64 s[26:27], s[26:27], exec
	s_waitcnt lgkmcnt(0)
	s_cselect_b32 s26, s8, s23
	s_cselect_b32 s27, s9, s63
	s_add_u32 s30, s26, 0x80
	s_addc_u32 s31, s27, 0
	s_barrier
	s_setprio 1
	s_waitcnt lgkmcnt(6)
	v_mfma_f32_16x16x128_f8f6f4 v[186:189], v[18:25], v[58:65], v[186:189]
	v_mfma_f32_16x16x128_f8f6f4 v[194:197], v[26:33], v[58:65], v[194:197]
	s_waitcnt lgkmcnt(4)
	v_mfma_f32_16x16x128_f8f6f4 v[190:193], v[18:25], v[50:57], v[190:193]
	v_mfma_f32_16x16x128_f8f6f4 v[182:185], v[26:33], v[50:57], v[182:185]
	s_waitcnt lgkmcnt(2)
	v_mfma_f32_16x16x128_f8f6f4 v[154:157], v[18:25], v[42:49], v[154:157]
	v_mfma_f32_16x16x128_f8f6f4 v[150:153], v[26:33], v[42:49], v[150:153]
	s_waitcnt lgkmcnt(0)
	v_mfma_f32_16x16x128_f8f6f4 v[138:141], v[18:25], v[34:41], v[138:141]
	v_mfma_f32_16x16x128_f8f6f4 v[134:137], v[26:33], v[34:41], v[134:137]
	v_mfma_f32_16x16x128_f8f6f4 v[174:177], v[2:9], v[58:65], v[174:177]
	v_mfma_f32_16x16x128_f8f6f4 v[178:181], v[10:17], v[58:65], v[178:181]
	v_mfma_f32_16x16x128_f8f6f4 v[170:173], v[2:9], v[50:57], v[170:173]
	v_mfma_f32_16x16x128_f8f6f4 v[166:169], v[10:17], v[50:57], v[166:169]
	v_mfma_f32_16x16x128_f8f6f4 v[162:165], v[2:9], v[42:49], v[162:165]
	v_mfma_f32_16x16x128_f8f6f4 v[158:161], v[10:17], v[42:49], v[158:161]
	v_mfma_f32_16x16x128_f8f6f4 v[146:149], v[2:9], v[34:41], v[146:149]
	v_mfma_f32_16x16x128_f8f6f4 v[142:145], v[10:17], v[34:41], v[142:145]
	s_setprio 0
	s_barrier
	ds_read_b128 v[34:37], v207 offset:16384
	ds_read_b128 v[38:41], v207 offset:17408
	ds_read_b128 v[42:45], v207 offset:18432
	ds_read_b128 v[46:49], v207 offset:19456
	ds_read_b128 v[50:53], v207 offset:20480
	ds_read_b128 v[54:57], v207 offset:21504
	ds_read_b128 v[58:61], v207 offset:22528
	ds_read_b128 v[62:65], v207 offset:23552
	s_add_i32 s66, s65, 0x10000
	s_mov_b32 m0, s66
	s_nop 0
	global_load_lds_dwordx4 v204, s[26:27]
	s_add_i32 s66, s65, 0x12000
	s_mov_b32 m0, s66
	s_nop 0
	global_load_lds_dwordx4 v205, s[26:27]
	s_add_u32 s66, s26, 0x2000
	s_addc_u32 s67, s27, 0
	s_add_i32 s68, s65, 0x14000
	s_mov_b32 m0, s68
	s_nop 0
	global_load_lds_dwordx4 v204, s[66:67]
	s_add_i32 s68, s65, 0x16000
	s_mov_b32 m0, s68
	s_nop 0
	global_load_lds_dwordx4 v205, s[66:67]
	s_waitcnt vmcnt(6)
	s_waitcnt lgkmcnt(0)
	s_barrier
	s_setprio 1
	s_waitcnt lgkmcnt(6)
	v_mfma_f32_16x16x128_f8f6f4 v[122:125], v[18:25], v[34:41], v[122:125]
	v_mfma_f32_16x16x128_f8f6f4 v[118:121], v[26:33], v[34:41], v[118:121]
	s_waitcnt lgkmcnt(4)
	v_mfma_f32_16x16x128_f8f6f4 v[106:109], v[18:25], v[42:49], v[106:109]
	v_mfma_f32_16x16x128_f8f6f4 v[102:105], v[26:33], v[42:49], v[102:105]
	s_waitcnt lgkmcnt(2)
	v_mfma_f32_16x16x128_f8f6f4 v[90:93], v[18:25], v[50:57], v[90:93]
	v_mfma_f32_16x16x128_f8f6f4 v[86:89], v[26:33], v[50:57], v[86:89]
	s_waitcnt lgkmcnt(0)
	v_mfma_f32_16x16x128_f8f6f4 v[74:77], v[18:25], v[58:65], v[74:77]
	v_mfma_f32_16x16x128_f8f6f4 v[70:73], v[26:33], v[58:65], v[70:73]
	v_mfma_f32_16x16x128_f8f6f4 v[130:133], v[2:9], v[34:41], v[130:133]
	v_mfma_f32_16x16x128_f8f6f4 v[126:129], v[10:17], v[34:41], v[126:129]
	v_mfma_f32_16x16x128_f8f6f4 v[114:117], v[2:9], v[42:49], v[114:117]
	v_mfma_f32_16x16x128_f8f6f4 v[110:113], v[10:17], v[42:49], v[110:113]
	v_mfma_f32_16x16x128_f8f6f4 v[98:101], v[2:9], v[50:57], v[98:101]
	v_mfma_f32_16x16x128_f8f6f4 v[94:97], v[10:17], v[50:57], v[94:97]
	v_mfma_f32_16x16x128_f8f6f4 v[82:85], v[2:9], v[58:65], v[82:85]
	v_mfma_f32_16x16x128_f8f6f4 v[78:81], v[10:17], v[58:65], v[78:81]
	s_setprio 0
	s_barrier
	s_mov_b32 m0, s65
	s_nop 0
	global_load_lds_dwordx4 v66, s[28:29]
	s_add_i32 s98, s65, 0x2000
	s_mov_b32 m0, s98
	s_nop 0
	global_load_lds_dwordx4 v67, s[28:29]
	v_add_u32_e32 v14, 0x18000, v206
	v_add_u32_e32 v30, 0x1c000, v206
	ds_read_b128 v[2:5], v14
	ds_read_b128 v[6:9], v14 offset:1024
	ds_read_b128 v[10:13], v14 offset:2048
	ds_read_b128 v[14:17], v14 offset:3072
	ds_read_b128 v[18:21], v30
	ds_read_b128 v[22:25], v30 offset:1024
	ds_read_b128 v[26:29], v30 offset:2048
	ds_read_b128 v[30:33], v30 offset:3072
	ds_read_b128 v[34:37], v207 offset:32768
	ds_read_b128 v[38:41], v207 offset:33792
	ds_read_b128 v[42:45], v207 offset:34816
	ds_read_b128 v[46:49], v207 offset:35840
	ds_read_b128 v[50:53], v207 offset:36864
	ds_read_b128 v[54:57], v207 offset:37888
	ds_read_b128 v[58:61], v207 offset:38912
	ds_read_b128 v[62:65], v207 offset:39936
	s_add_i32 s66, s65, 0x4000
	s_mov_b32 m0, s66
	s_nop 0
	global_load_lds_dwordx4 v68, s[28:29]
	s_add_i32 s66, s65, 0x6000
	s_mov_b32 m0, s66
	s_nop 0
	global_load_lds_dwordx4 v69, s[28:29]
	s_waitcnt vmcnt(8)
	s_waitcnt lgkmcnt(0)
	s_barrier
; #define PG8_STAGE(bufoff, gbase, voff) do { PG8_GLDS((const char*)(gbase), (voff)[0], ldsb + (bufoff)); PG8_GLDS((const char*)(gbase), (voff)[1], ldsb + (bufoff) + 8192u); } while (0)
; #define PG8_STAGEA(bufoff, gbase, o0, o1) do { PG8_GLDS((const char*)(gbase), (o0), ldsb + (bufoff)); PG8_GLDS((const char*)(gbase), (o1), ldsb + (bufoff) + 8192u); } while (0)
; #define PG8_STAGEA1(bufoff, gbase) do { if constexpr (Sched::GATHER) { PG8_STAGEA(bufoff, gbase, vA2, vA3); } else { PG8_STAGEA(bufoff, (gbase) + hstep, vA0, vA1); } } while (0)
; #define PG8_WAIT_VR() PG8_WAIT_V(8)
; #define PG8_WAIT_L(n) asm volatile("s_waitcnt lgkmcnt(" #n ")" ::: "memory")
; template <class Epi, class Sched, bool F8 = false, bool PF = false, bool I8 = false, int PID = -1>
; __device__ __forceinline__ void gemm_phase(LAS unsigned char* lds, LAS unsigned char* xlds, const int RP, const int RPB, const int nt, const Sched& S, const Epi& E, const int stagger_ticks) {
;     ...
;         for (int t = 0; t < nt; t += 2) {
;             const bool last = (t == nt - 2);
;             unsigned ldsb = ldsb0; asm volatile("" : "+s"(ldsb));
;             const char* a1 = cA + (size_t)(t + 1) * kstep;
;             const char* a2 = last ? nA : cA + (size_t)(t + 2) * kstep; const char* b2 = last ? nB : cB + (size_t)(t + 2) * kstep;
;             const char* a3 = a2 + kstep; const char* b3 = b2 + kstep;
;             if constexpr (PF) { const char* pfa = (t + 4 < nt) ? cA + (size_t)(t + 4) * kstep : nA + (size_t)(t + 4 - nt) * kstep;
;                 asm volatile("s_mov_b32 m0, %2\n\ts_nop 0\n\tglobal_load_lds_dword %0, %1" :: "v"(voffP), "s"(pfa), "s"(ldsP) : "memory", "m0"); }
;             const bool relax = (Epi::RELAX > 0) && (t == 0) && epi_ran;
;             PG8_LDB(B0, 0, 0); PG8_LDB(B1, 0, 1); PG8_SCHED; PG8_LDA(At, 0, 0); PG8_STAGEA1(PG8_SA(1, 1), a1);
;     ...
;             PG8_LDB(B0, 1, 0); PG8_LDB(B1, 1, 1); PG8_SCHED; PG8_LDA(At, 1, 0); PG8_STAGEA1(PG8_SA(0, 1), a2);
;             PG8_WAIT_VR(); PG8_WAIT_L(0); PG8_BAR; PG8_MMA(0, 0, At, B0); PG8_MMA(0, 1, At, B1); PG8_BAR; PG8_SCHED;
;             PG8_LDA(At, 1, 1); PG8_STAGE(PG8_SB(1, 0), b3, voffB); PG8_STAGE(PG8_SB(1, 1), b3 + hstepB, voffB); PG8_STAGEA(PG8_SA(1, 0), a3, vA0, vA1);
;             PG8_WAIT_VR(); PG8_WAIT_L(0); PG8_BAR; PG8_MMA(1, 0, At, B0); PG8_MMA(1, 1, At, B1); PG8_BAR; PG8_SCHED;
	s_setprio 1
	s_waitcnt lgkmcnt(6)
	v_mfma_f32_16x16x128_f8f6f4 v[186:189], v[2:9], v[34:41], v[186:189]
	v_mfma_f32_16x16x128_f8f6f4 v[194:197], v[10:17], v[34:41], v[194:197]
	s_waitcnt lgkmcnt(4)
	v_mfma_f32_16x16x128_f8f6f4 v[190:193], v[2:9], v[42:49], v[190:193]
	v_mfma_f32_16x16x128_f8f6f4 v[182:185], v[10:17], v[42:49], v[182:185]
	s_waitcnt lgkmcnt(2)
	v_mfma_f32_16x16x128_f8f6f4 v[154:157], v[2:9], v[50:57], v[154:157]
	v_mfma_f32_16x16x128_f8f6f4 v[150:153], v[10:17], v[50:57], v[150:153]
	s_waitcnt lgkmcnt(0)
	v_mfma_f32_16x16x128_f8f6f4 v[138:141], v[2:9], v[58:65], v[138:141]
	v_mfma_f32_16x16x128_f8f6f4 v[134:137], v[10:17], v[58:65], v[134:137]
	v_mfma_f32_16x16x128_f8f6f4 v[174:177], v[18:25], v[34:41], v[174:177]
	v_mfma_f32_16x16x128_f8f6f4 v[178:181], v[26:33], v[34:41], v[178:181]
	v_mfma_f32_16x16x128_f8f6f4 v[170:173], v[18:25], v[42:49], v[170:173]
	v_mfma_f32_16x16x128_f8f6f4 v[166:169], v[26:33], v[42:49], v[166:169]
	v_mfma_f32_16x16x128_f8f6f4 v[162:165], v[18:25], v[50:57], v[162:165]
	v_mfma_f32_16x16x128_f8f6f4 v[158:161], v[26:33], v[50:57], v[158:161]
	v_mfma_f32_16x16x128_f8f6f4 v[146:149], v[18:25], v[58:65], v[146:149]
	v_mfma_f32_16x16x128_f8f6f4 v[142:145], v[26:33], v[58:65], v[142:145]
	s_setprio 0
	s_barrier
	ds_read_b128 v[34:37], v207 offset:49152
	ds_read_b128 v[38:41], v207 offset:50176
	ds_read_b128 v[42:45], v207 offset:51200
	ds_read_b128 v[46:49], v207 offset:52224
	ds_read_b128 v[50:53], v207 offset:53248
	ds_read_b128 v[54:57], v207 offset:54272
	ds_read_b128 v[58:61], v207 offset:55296
	ds_read_b128 v[62:65], v207 offset:56320
	s_add_i32 s28, s65, 0x18000
	s_mov_b32 m0, s28
	s_nop 0
	global_load_lds_dwordx4 v204, s[30:31]
	s_add_i32 s28, s65, 0x1a000
	s_mov_b32 m0, s28
	s_nop 0
	global_load_lds_dwordx4 v205, s[30:31]
	s_add_u32 s26, s26, 0x2080
	s_addc_u32 s27, s27, 0
	s_add_i32 s28, s65, 0x1c000
	s_mov_b32 m0, s28
	s_nop 0
	global_load_lds_dwordx4 v204, s[26:27]
	s_add_i32 s28, s65, 0x1e000
	s_mov_b32 m0, s28
	s_nop 0
	global_load_lds_dwordx4 v205, s[26:27]
	s_waitcnt vmcnt(6)
	s_waitcnt lgkmcnt(0)
	s_barrier
	s_setprio 1
	s_waitcnt lgkmcnt(6)
	v_mfma_f32_16x16x128_f8f6f4 v[122:125], v[2:9], v[34:41], v[122:125]
	v_mfma_f32_16x16x128_f8f6f4 v[118:121], v[10:17], v[34:41], v[118:121]
	s_waitcnt lgkmcnt(4)
	v_mfma_f32_16x16x128_f8f6f4 v[106:109], v[2:9], v[42:49], v[106:109]
	v_mfma_f32_16x16x128_f8f6f4 v[102:105], v[10:17], v[42:49], v[102:105]
	s_waitcnt lgkmcnt(2)
	v_mfma_f32_16x16x128_f8f6f4 v[90:93], v[2:9], v[50:57], v[90:93]
	v_mfma_f32_16x16x128_f8f6f4 v[86:89], v[10:17], v[50:57], v[86:89]
	s_waitcnt lgkmcnt(0)
	v_mfma_f32_16x16x128_f8f6f4 v[74:77], v[2:9], v[58:65], v[74:77]
	v_mfma_f32_16x16x128_f8f6f4 v[70:73], v[10:17], v[58:65], v[70:73]
	v_mfma_f32_16x16x128_f8f6f4 v[130:133], v[18:25], v[34:41], v[130:133]
	v_mfma_f32_16x16x128_f8f6f4 v[126:129], v[26:33], v[34:41], v[126:129]
	v_mfma_f32_16x16x128_f8f6f4 v[114:117], v[18:25], v[42:49], v[114:117]
	v_mfma_f32_16x16x128_f8f6f4 v[110:113], v[26:33], v[42:49], v[110:113]
	v_mfma_f32_16x16x128_f8f6f4 v[98:101], v[18:25], v[50:57], v[98:101]
	v_mfma_f32_16x16x128_f8f6f4 v[94:97], v[26:33], v[50:57], v[94:97]
	v_mfma_f32_16x16x128_f8f6f4 v[82:85], v[18:25], v[58:65], v[82:85]
	v_mfma_f32_16x16x128_f8f6f4 v[78:81], v[26:33], v[58:65], v[78:81]
	s_setprio 0
	s_barrier
	s_add_i32 s64, s64, 2
	s_add_u32 s23, s23, 0x100
	s_addc_u32 s63, s63, 0
	s_add_u32 s2, s2, 0x100
	s_addc_u32 s3, s3, 0
	s_cmp_gt_u32 s64, 5
	s_cbranch_scc1 .LBB0_961
.LBB0_959:
	s_mov_b32 s65, s42
	s_add_i32 s98, s65, 0x8000
	s_mov_b32 m0, s98
	s_nop 0
	global_load_lds_dwordx4 v66, s[2:3]
	s_add_i32 s98, s65, 0xa000
	s_mov_b32 m0, s98
	s_nop 0
	global_load_lds_dwordx4 v67, s[2:3]
	v_add_u32_e32 v2, 0x10000, v206
	v_add_u32_e32 v14, 0x14000, v206
	ds_read_b128 v[18:21], v2
	ds_read_b128 v[22:25], v2 offset:1024
	ds_read_b128 v[26:29], v2 offset:2048
	ds_read_b128 v[30:33], v2 offset:3072
	ds_read_b128 v[2:5], v14
	ds_read_b128 v[6:9], v14 offset:1024
	ds_read_b128 v[10:13], v14 offset:2048
	ds_read_b128 v[14:17], v14 offset:3072
	s_cmp_eq_u32 s64, 4
	s_cselect_b64 s[26:27], -1, 0
	s_add_i32 s24, s65, 0xc000
	s_add_i32 s25, s65, 0xe000
	s_cmp_lg_u32 s64, 4
	ds_read_b128 v[58:61], v207
	ds_read_b128 v[62:65], v207 offset:1024
	ds_read_b128 v[50:53], v207 offset:2048
	ds_read_b128 v[54:57], v207 offset:3072
	ds_read_b128 v[42:45], v207 offset:4096
	ds_read_b128 v[46:49], v207 offset:5120
	ds_read_b128 v[34:37], v207 offset:6144
	ds_read_b128 v[38:41], v207 offset:7168
	s_mov_b32 m0, s24
	s_nop 0
	global_load_lds_dwordx4 v68, s[2:3]
	s_nop 0
	s_mov_b32 m0, s25
	s_nop 0
	global_load_lds_dwordx4 v69, s[2:3]
	s_cbranch_scc1 .LBB0_958
	ds_read_b128 v[66:69], v203
	s_branch .LBB0_958

; #define PG8_STAGE(bufoff, gbase, voff) do { PG8_GLDS((const char*)(gbase), (voff)[0], ldsb + (bufoff)); PG8_GLDS((const char*)(gbase), (voff)[1], ldsb + (bufoff) + 8192u); } while (0)
; #define PG8_STAGEA(bufoff, gbase, o0, o1) do { PG8_GLDS((const char*)(gbase), (o0), ldsb + (bufoff)); PG8_GLDS((const char*)(gbase), (o1), ldsb + (bufoff) + 8192u); } while (0)
; #define PG8_STAGEA1(bufoff, gbase) do { if constexpr (Sched::GATHER) { PG8_STAGEA(bufoff, gbase, vA2, vA3); } else { PG8_STAGEA(bufoff, (gbase) + hstep, vA0, vA1); } } while (0)
; #define PG8_LDA(dst, b, h) do { if constexpr (F8) { _Pragma("unroll") for (int m = 0; m < 4; ++m) dst##8[m] = PG8_LD32(lds + PG8_SA(b, h) + aoff + m * 2048); } else { \
;         _Pragma("unroll") for (int m = 0; m < 4; ++m) _Pragma("unroll") for (int k = 0; k < 2; ++k) dst[m][k] = *(const LAS bf16x8*)(lds + PG8_SA(b, h) + aoff + m * 2048 + k * 1024); } } while (0)
; #define PG8_WAIT_VX() do { if (relax) asm volatile("s_waitcnt vmcnt(%0)" :: "n"(8 + Epi::RELAX) : "memory"); else PG8_WAIT_V(8); } while (0)
; #define PG8_WAIT_L(n) asm volatile("s_waitcnt lgkmcnt(" #n ")" ::: "memory")
; #define PG8_BAR __builtin_amdgcn_s_barrier()
; template <class Epi, class Sched, bool F8 = false, bool PF = false, bool I8 = false, int PID = -1>
; __device__ __forceinline__ void gemm_phase(LAS unsigned char* lds, LAS unsigned char* xlds, const int RP, const int RPB, const int nt, const Sched& S, const Epi& E, const int stagger_ticks) {
;     ...
;             PG8_LDB(B0, 0, 0); PG8_LDB(B1, 0, 1); PG8_SCHED; PG8_LDA(At, 0, 0); PG8_STAGEA1(PG8_SA(1, 1), a1);
;             if (Sched::GATHER) { if (last) { const u32x4 nv = *nslot; vA0 = nv.x; vA1 = nv.y; vA2 = nv.z; vA3 = nv.w; } }
;             PG8_WAIT_VX(); PG8_WAIT_L(0); PG8_BAR; PG8_MMA(0, 0, At, B0); PG8_MMA(0, 1, At, B1); PG8_BAR; PG8_SCHED;
;             if constexpr (Epi::BIAS_DMA) { if (t == 0 && has_next) E.bias_dma(nxt, xlds + 8192 + ((ui + 1) & 1) * Epi::BIAS_STRIDE, wid, lane); }
;             PG8_LDA(At, 0, 1); PG8_STAGE(PG8_SB(0, 0), b2, voffB); PG8_STAGE(PG8_SB(0, 1), b2 + hstepB, voffB); PG8_STAGEA(PG8_SA(0, 0), a2, vA0, vA1);
;             PG8_WAIT_VX(); PG8_WAIT_L(0); PG8_BAR; PG8_MMA(1, 0, At, B0); PG8_MMA(1, 1, At, B1); PG8_BAR; PG8_SCHED;
;             PG8_LDB(B0, 1, 0); PG8_LDB(B1, 1, 1); PG8_SCHED; PG8_LDA(At, 1, 0); PG8_STAGEA1(PG8_SA(0, 1), a2);
.Lmy_z958:
	s_add_u32 s28, s2, 0x80
	s_addc_u32 s29, s3, 0
	s_and_b64 s[24:25], s[26:27], exec
	s_cselect_b32 s28, s20, s28
	s_cselect_b32 s29, s21, s29
	s_add_u32 s24, s28, 0x80
	s_addc_u32 s25, s29, 0
	s_waitcnt vmcnt(8)
	s_and_b64 s[26:27], s[26:27], exec
	s_waitcnt lgkmcnt(0)
	s_cselect_b32 s26, s8, s23
	s_cselect_b32 s27, s9, s63
	s_add_u32 s30, s26, 0x80
	s_addc_u32 s31, s27, 0
	s_barrier
	s_setprio 1
	s_waitcnt lgkmcnt(6)
	v_mfma_f32_16x16x128_f8f6f4 v[186:189], v[18:25], v[58:65], 0
	v_mfma_f32_16x16x128_f8f6f4 v[194:197], v[26:33], v[58:65], 0
	s_waitcnt lgkmcnt(4)
	v_mfma_f32_16x16x128_f8f6f4 v[190:193], v[18:25], v[50:57], 0
	v_mfma_f32_16x16x128_f8f6f4 v[182:185], v[26:33], v[50:57], 0
	s_waitcnt lgkmcnt(2)
	v_mfma_f32_16x16x128_f8f6f4 v[154:157], v[18:25], v[42:49], 0
	v_mfma_f32_16x16x128_f8f6f4 v[150:153], v[26:33], v[42:49], 0
	s_waitcnt lgkmcnt(0)
	v_mfma_f32_16x16x128_f8f6f4 v[138:141], v[18:25], v[34:41], 0
	v_mfma_f32_16x16x128_f8f6f4 v[134:137], v[26:33], v[34:41], 0
	v_mfma_f32_16x16x128_f8f6f4 v[174:177], v[2:9], v[58:65], 0
	v_mfma_f32_16x16x128_f8f6f4 v[178:181], v[10:17], v[58:65], 0
	v_mfma_f32_16x16x128_f8f6f4 v[170:173], v[2:9], v[50:57], 0
	v_mfma_f32_16x16x128_f8f6f4 v[166:169], v[10:17], v[50:57], 0
	v_mfma_f32_16x16x128_f8f6f4 v[162:165], v[2:9], v[42:49], 0
	v_mfma_f32_16x16x128_f8f6f4 v[158:161], v[10:17], v[42:49], 0
	v_mfma_f32_16x16x128_f8f6f4 v[146:149], v[2:9], v[34:41], 0
	v_mfma_f32_16x16x128_f8f6f4 v[142:145], v[10:17], v[34:41], 0
	s_setprio 0
	s_barrier
	ds_read_b128 v[34:37], v207 offset:16384
	ds_read_b128 v[38:41], v207 offset:17408
	ds_read_b128 v[42:45], v207 offset:18432
	ds_read_b128 v[46:49], v207 offset:19456
	ds_read_b128 v[50:53], v207 offset:20480
	ds_read_b128 v[54:57], v207 offset:21504
	ds_read_b128 v[58:61], v207 offset:22528
	ds_read_b128 v[62:65], v207 offset:23552
	s_add_i32 s66, s65, 0x10000
	s_mov_b32 m0, s66
	s_nop 0
	global_load_lds_dwordx4 v204, s[26:27]
	s_add_i32 s66, s65, 0x12000
	s_mov_b32 m0, s66
	s_nop 0
	global_load_lds_dwordx4 v205, s[26:27]
	s_add_u32 s66, s26, 0x2000
	s_addc_u32 s67, s27, 0
	s_add_i32 s68, s65, 0x14000
	s_mov_b32 m0, s68
	s_nop 0
	global_load_lds_dwordx4 v204, s[66:67]
	s_add_i32 s68, s65, 0x16000
	s_mov_b32 m0, s68
	s_nop 0
	global_load_lds_dwordx4 v205, s[66:67]
	s_waitcnt vmcnt(6)
	s_waitcnt lgkmcnt(0)
	s_barrier
	s_setprio 1
	s_waitcnt lgkmcnt(6)
	v_mfma_f32_16x16x128_f8f6f4 v[122:125], v[18:25], v[34:41], 0
	v_mfma_f32_16x16x128_f8f6f4 v[118:121], v[26:33], v[34:41], 0
	s_waitcnt lgkmcnt(4)
	v_mfma_f32_16x16x128_f8f6f4 v[106:109], v[18:25], v[42:49], 0
	v_mfma_f32_16x16x128_f8f6f4 v[102:105], v[26:33], v[42:49], 0
	s_waitcnt lgkmcnt(2)
	v_mfma_f32_16x16x128_f8f6f4 v[90:93], v[18:25], v[50:57], 0
	v_mfma_f32_16x16x128_f8f6f4 v[86:89], v[26:33], v[50:57], 0
	s_waitcnt lgkmcnt(0)
	v_mfma_f32_16x16x128_f8f6f4 v[74:77], v[18:25], v[58:65], 0
	v_mfma_f32_16x16x128_f8f6f4 v[70:73], v[26:33], v[58:65], 0
	v_mfma_f32_16x16x128_f8f6f4 v[130:133], v[2:9], v[34:41], 0
	v_mfma_f32_16x16x128_f8f6f4 v[126:129], v[10:17], v[34:41], 0
	v_mfma_f32_16x16x128_f8f6f4 v[114:117], v[2:9], v[42:49], 0
	v_mfma_f32_16x16x128_f8f6f4 v[110:113], v[10:17], v[42:49], 0
	v_mfma_f32_16x16x128_f8f6f4 v[98:101], v[2:9], v[50:57], 0
	v_mfma_f32_16x16x128_f8f6f4 v[94:97], v[10:17], v[50:57], 0
	v_mfma_f32_16x16x128_f8f6f4 v[82:85], v[2:9], v[58:65], 0
	v_mfma_f32_16x16x128_f8f6f4 v[78:81], v[10:17], v[58:65], 0
	s_setprio 0
	s_barrier
	s_mov_b32 m0, s65
	s_nop 0
	global_load_lds_dwordx4 v66, s[28:29]
	s_add_i32 s98, s65, 0x2000
	s_mov_b32 m0, s98
	s_nop 0
	global_load_lds_dwordx4 v67, s[28:29]
	v_pk_fma_f32 v[218:219], v[218:219], v[238:239], v[238:239] op_sel:[0,0,1] op_sel_hi:[1,0,1]
	v_pk_fma_f32 v[220:221], v[220:221], v[238:239], v[238:239] op_sel:[0,0,1] op_sel_hi:[1,0,1]
	v_pk_fma_f32 v[222:223], v[222:223], v[238:239], v[238:239] op_sel:[0,0,1] op_sel_hi:[1,0,1]
	v_pk_fma_f32 v[224:225], v[224:225], v[238:239], v[238:239] op_sel:[0,0,1] op_sel_hi:[1,0,1]
	v_pk_fma_f32 v[214:215], v[214:215], v[240:241], v[240:241] op_sel:[0,0,1] op_sel_hi:[1,0,1]
	v_pk_fma_f32 v[216:217], v[216:217], v[240:241], v[240:241] op_sel:[0,0,1] op_sel_hi:[1,0,1]
	v_pk_fma_f32 v[226:227], v[226:227], v[240:241], v[240:241] op_sel:[0,0,1] op_sel_hi:[1,0,1]
	v_pk_fma_f32 v[228:229], v[228:229], v[240:241], v[240:241] op_sel:[0,0,1] op_sel_hi:[1,0,1]
	v_add_u32_e32 v14, 0x18000, v206
	v_add_u32_e32 v30, 0x1c000, v206
	ds_read_b128 v[2:5], v14
	ds_read_b128 v[6:9], v14 offset:1024
	ds_read_b128 v[10:13], v14 offset:2048
	ds_read_b128 v[14:17], v14 offset:3072
	ds_read_b128 v[18:21], v30
	ds_read_b128 v[22:25], v30 offset:1024
	ds_read_b128 v[26:29], v30 offset:2048
	ds_read_b128 v[30:33], v30 offset:3072
	ds_read_b128 v[34:37], v207 offset:32768
	ds_read_b128 v[38:41], v207 offset:33792
	ds_read_b128 v[42:45], v207 offset:34816
	ds_read_b128 v[46:49], v207 offset:35840
	ds_read_b128 v[50:53], v207 offset:36864
	ds_read_b128 v[54:57], v207 offset:37888
	ds_read_b128 v[58:61], v207 offset:38912
	ds_read_b128 v[62:65], v207 offset:39936
	s_add_i32 s66, s65, 0x4000
	s_mov_b32 m0, s66
	s_nop 0
	global_load_lds_dwordx4 v68, s[28:29]
	s_add_i32 s66, s65, 0x6000
	s_mov_b32 m0, s66
	s_nop 0
	global_load_lds_dwordx4 v69, s[28:29]
	s_waitcnt vmcnt(8)
	s_waitcnt lgkmcnt(0)
	s_barrier
; #define PG8_STAGE(bufoff, gbase, voff) do { PG8_GLDS((const char*)(gbase), (voff)[0], ldsb + (bufoff)); PG8_GLDS((const char*)(gbase), (voff)[1], ldsb + (bufoff) + 8192u); } while (0)
; #define PG8_STAGEA(bufoff, gbase, o0, o1) do { PG8_GLDS((const char*)(gbase), (o0), ldsb + (bufoff)); PG8_GLDS((const char*)(gbase), (o1), ldsb + (bufoff) + 8192u); } while (0)
; #define PG8_LDA(dst, b, h) do { if constexpr (F8) { _Pragma("unroll") for (int m = 0; m < 4; ++m) dst##8[m] = PG8_LD32(lds + PG8_SA(b, h) + aoff + m * 2048); } else { \
;         _Pragma("unroll") for (int m = 0; m < 4; ++m) _Pragma("unroll") for (int k = 0; k < 2; ++k) dst[m][k] = *(const LAS bf16x8*)(lds + PG8_SA(b, h) + aoff + m * 2048 + k * 1024); } } while (0)
; #define PG8_WAIT_VR() PG8_WAIT_V(8)
; #define PG8_WAIT_L(n) asm volatile("s_waitcnt lgkmcnt(" #n ")" ::: "memory")
; #define PG8_BAR __builtin_amdgcn_s_barrier()
; #define PG8_SCHED __builtin_amdgcn_sched_barrier(0)
; template <class Epi, class Sched, bool F8 = false, bool PF = false, bool I8 = false, int PID = -1>
; __device__ __forceinline__ void gemm_phase(LAS unsigned char* lds, LAS unsigned char* xlds, const int RP, const int RPB, const int nt, const Sched& S, const Epi& E, const int stagger_ticks) {
;     ...
;             PG8_WAIT_VR(); PG8_WAIT_L(0); PG8_BAR; PG8_MMA(0, 0, At, B0); PG8_MMA(0, 1, At, B1); PG8_BAR; PG8_SCHED;
;             PG8_LDA(At, 1, 1); PG8_STAGE(PG8_SB(1, 0), b3, voffB); PG8_STAGE(PG8_SB(1, 1), b3 + hstepB, voffB); PG8_STAGEA(PG8_SA(1, 0), a3, vA0, vA1);
;             PG8_WAIT_VR(); PG8_WAIT_L(0); PG8_BAR; PG8_MMA(1, 0, At, B0); PG8_MMA(1, 1, At, B1); PG8_BAR; PG8_SCHED;
	s_setprio 1
	s_waitcnt lgkmcnt(6)
	v_mfma_f32_16x16x128_f8f6f4 v[186:189], v[2:9], v[34:41], v[186:189]
	v_mfma_f32_16x16x128_f8f6f4 v[194:197], v[10:17], v[34:41], v[194:197]
	s_waitcnt lgkmcnt(4)
	v_mfma_f32_16x16x128_f8f6f4 v[190:193], v[2:9], v[42:49], v[190:193]
	v_mfma_f32_16x16x128_f8f6f4 v[182:185], v[10:17], v[42:49], v[182:185]
	s_waitcnt lgkmcnt(2)
	v_mfma_f32_16x16x128_f8f6f4 v[154:157], v[2:9], v[50:57], v[154:157]
	v_mfma_f32_16x16x128_f8f6f4 v[150:153], v[10:17], v[50:57], v[150:153]
	s_waitcnt lgkmcnt(0)
	v_mfma_f32_16x16x128_f8f6f4 v[138:141], v[2:9], v[58:65], v[138:141]
	v_mfma_f32_16x16x128_f8f6f4 v[134:137], v[10:17], v[58:65], v[134:137]
	v_mfma_f32_16x16x128_f8f6f4 v[174:177], v[18:25], v[34:41], v[174:177]
	v_mfma_f32_16x16x128_f8f6f4 v[178:181], v[26:33], v[34:41], v[178:181]
	v_mfma_f32_16x16x128_f8f6f4 v[170:173], v[18:25], v[42:49], v[170:173]
	v_mfma_f32_16x16x128_f8f6f4 v[166:169], v[26:33], v[42:49], v[166:169]
	v_mfma_f32_16x16x128_f8f6f4 v[162:165], v[18:25], v[50:57], v[162:165]
	v_mfma_f32_16x16x128_f8f6f4 v[158:161], v[26:33], v[50:57], v[158:161]
	v_mfma_f32_16x16x128_f8f6f4 v[146:149], v[18:25], v[58:65], v[146:149]
	v_mfma_f32_16x16x128_f8f6f4 v[142:145], v[26:33], v[58:65], v[142:145]
	s_setprio 0
	s_barrier
	ds_read_b128 v[34:37], v207 offset:49152
	ds_read_b128 v[38:41], v207 offset:50176
	ds_read_b128 v[42:45], v207 offset:51200
	ds_read_b128 v[46:49], v207 offset:52224
	ds_read_b128 v[50:53], v207 offset:53248
	ds_read_b128 v[54:57], v207 offset:54272
	ds_read_b128 v[58:61], v207 offset:55296
	ds_read_b128 v[62:65], v207 offset:56320
	s_add_i32 s28, s65, 0x18000
	s_mov_b32 m0, s28
	s_nop 0
	global_load_lds_dwordx4 v204, s[30:31]
	s_add_i32 s28, s65, 0x1a000
	s_mov_b32 m0, s28
	s_nop 0
	global_load_lds_dwordx4 v205, s[30:31]
	s_add_u32 s26, s26, 0x2080
	s_addc_u32 s27, s27, 0
	s_add_i32 s28, s65, 0x1c000
	s_mov_b32 m0, s28
	s_nop 0
	global_load_lds_dwordx4 v204, s[26:27]
	s_add_i32 s28, s65, 0x1e000
	s_mov_b32 m0, s28
	s_nop 0
	global_load_lds_dwordx4 v205, s[26:27]
	s_waitcnt vmcnt(6)
	s_waitcnt lgkmcnt(0)
	s_barrier
	s_setprio 1
	s_waitcnt lgkmcnt(6)
	v_mfma_f32_16x16x128_f8f6f4 v[122:125], v[2:9], v[34:41], v[122:125]
	v_mfma_f32_16x16x128_f8f6f4 v[118:121], v[10:17], v[34:41], v[118:121]
	s_waitcnt lgkmcnt(4)
	v_mfma_f32_16x16x128_f8f6f4 v[106:109], v[2:9], v[42:49], v[106:109]
	v_mfma_f32_16x16x128_f8f6f4 v[102:105], v[10:17], v[42:49], v[102:105]
	s_waitcnt lgkmcnt(2)
	v_mfma_f32_16x16x128_f8f6f4 v[90:93], v[2:9], v[50:57], v[90:93]
	v_mfma_f32_16x16x128_f8f6f4 v[86:89], v[10:17], v[50:57], v[86:89]
	s_waitcnt lgkmcnt(0)
	v_mfma_f32_16x16x128_f8f6f4 v[74:77], v[2:9], v[58:65], v[74:77]
	v_mfma_f32_16x16x128_f8f6f4 v[70:73], v[10:17], v[58:65], v[70:73]
	v_mfma_f32_16x16x128_f8f6f4 v[130:133], v[18:25], v[34:41], v[130:133]
	v_mfma_f32_16x16x128_f8f6f4 v[126:129], v[26:33], v[34:41], v[126:129]
	v_mfma_f32_16x16x128_f8f6f4 v[114:117], v[18:25], v[42:49], v[114:117]
	v_mfma_f32_16x16x128_f8f6f4 v[110:113], v[26:33], v[42:49], v[110:113]
	v_mfma_f32_16x16x128_f8f6f4 v[98:101], v[18:25], v[50:57], v[98:101]
	v_mfma_f32_16x16x128_f8f6f4 v[94:97], v[26:33], v[50:57], v[94:97]
	v_mfma_f32_16x16x128_f8f6f4 v[82:85], v[18:25], v[58:65], v[82:85]
	v_mfma_f32_16x16x128_f8f6f4 v[78:81], v[26:33], v[58:65], v[78:81]
	s_setprio 0
	s_barrier
	s_add_i32 s64, s64, 2
	s_add_u32 s23, s23, 0x100
	s_addc_u32 s63, s63, 0
	s_add_u32 s2, s2, 0x100
	s_addc_u32 s3, s3, 0
	s_cmp_gt_u32 s64, 5
	s_branch .LBB0_959
